# LN2 row loop: the 4 gate-vector loads per row cached in registers, re-loaded only when the row's sample changes
# speedup vs baseline: 1.0103x; 1.0018x over previous
; #define GAS __attribute__((address_space(1)))
; __device__ __forceinline__ void ph_ln2(Frame& F, int l, int ntok, bool last) {
;     const int gw = F.wg * NWAVES + F.wave, NGW = F.G * NWAVES;
;     const int cA = 256 * (F.lane >> 4) + 32 * ((F.lane >> 2) & 3) + 8 * (F.lane & 3);
;     ...
;     const float* lg = F.in[I_LN2G] + l * DM; const float* lb = F.in[I_LN2B] + l * DM;
;     struct Ln2Raw { u32x2 q[8]; u32x4 qs, xa, xb; };
;     auto ln2_load = [&](int row) { Ln2Raw r;
;         const unsigned char* y2 = (const unsigned char*)(F.ws + WS_Y2) + (size_t)row * 5120;
;         const bf16_t* xr = (const bf16_t*)(F.ws + WS_XR) + (size_t)row * DM;
; #pragma unroll
;         for (int k = 0; k < 8; ++k) r.q[k] = __builtin_nontemporal_load((const GAS u32x2*)(y2 + k * 512 + 8 * F.lane));
;         r.qs = __builtin_nontemporal_load((const GAS u32x4*)(y2 + 4096 + 16 * F.lane));
;         r.xa = __builtin_nontemporal_load((const GAS u32x4*)(xr + cA)); r.xb = __builtin_nontemporal_load((const GAS u32x4*)(xr + cA + 128));
;         return r; };
;     Ln2Raw cur = ln2_load(gw < ntok ? gw : 0);
.LBB0_1687:
	v_readlane_b32 s36, v252, 8
	s_mov_b32 s0, s97
	v_readlane_b32 s38, v252, 10
	v_readlane_b32 s39, v252, 11
	v_readlane_b32 s4, v254, 28
	v_mbcnt_lo_u32_b32 v8, -1, 0
	v_mbcnt_hi_u32_b32 v8, -1, v8
	v_readlane_b32 s37, v252, 9
	s_mov_b64 s[20:21], s[38:39]
	s_add_i32 s38, s0, s4
	s_mov_b64 s[2:3], s[36:37]
	s_cmp_ge_i32 s38, s80
	s_cbranch_scc1 .LBB0_1696
	s_lshl_b32 s22, s30, 10
	v_readlane_b32 s40, v252, 0
	s_lshl_b64 s[4:5], s[22:23], 2
	v_readlane_b32 s46, v252, 6
	v_readlane_b32 s47, v252, 7
	s_add_u32 s18, s46, s4
	v_readlane_b32 s44, v252, 4
	s_addc_u32 s19, s47, s5
	v_readlane_b32 s45, v252, 5
	s_add_u32 s4, s44, s4
	s_addc_u32 s5, s45, s5
	s_add_u32 s36, s20, 0x64000000
	v_lshlrev_b32_e32 v34, 3, v8
	v_readlane_b32 s42, v252, 2
	v_readlane_b32 s43, v252, 3
	s_addc_u32 s37, s21, 0
	s_ashr_i32 s39, s38, 31
	v_lshlrev_b32_e32 v32, 4, v8
	v_and_b32_e32 v0, 0x78, v34
	s_movk_i32 s0, 0xff00
	s_lshl_b64 s[42:43], s[38:39], 11
	v_and_or_b32 v36, v32, s0, v0
	v_readlane_b32 s41, v252, 1
	s_add_u32 s40, s36, s42
	v_ashrrev_i32_e32 v37, 31, v36
	s_addc_u32 s41, s37, s43
	v_lshlrev_b64 v[10:11], 1, v[36:37]
	s_add_u32 s22, s20, 0x2f600000
	v_lshl_add_u64 v[0:1], s[40:41], 0, v[10:11]
	s_addc_u32 s44, s21, 0
	s_mul_i32 s40, s38, 0x1400
	s_mul_hi_i32 s0, s38, 0x1400
	s_add_u32 s40, s22, s40
	s_addc_u32 s41, s44, s0
	v_ashrrev_i32_e32 v33, 31, v32
	s_waitcnt vmcnt(0)
	v_lshl_add_u64 v[4:5], s[40:41], 0, v[32:33]
	s_movk_i32 s0, 0x1000
	v_add_co_u32_e32 v4, vcc, s0, v4
	v_ashrrev_i32_e32 v35, 31, v34
	s_nop 0
	v_addc_co_u32_e32 v5, vcc, 0, v5, vcc
	v_lshl_add_u64 v[16:17], s[40:41], 0, v[34:35]
	global_load_dwordx4 v[12:15], v[0:1], off offset:256 nt
	s_nop 0
	global_load_dwordx4 v[0:3], v[0:1], off nt
	s_nop 0
	global_load_dwordx2 v[66:67], v[16:17], off offset:3584 nt
	global_load_dwordx2 v[64:65], v[16:17], off offset:3072 nt
	global_load_dwordx2 v[62:63], v[16:17], off offset:2560 nt
	global_load_dwordx2 v[60:61], v[16:17], off offset:2048 nt
	global_load_dwordx2 v[58:59], v[16:17], off offset:1536 nt
	global_load_dwordx2 v[56:57], v[16:17], off offset:1024 nt
	global_load_dwordx2 v[54:55], v[16:17], off offset:512 nt
	s_nop 0
	global_load_dwordx4 v[4:7], v[4:5], off nt
	s_nop 0
	global_load_dwordx2 v[52:53], v[16:17], off nt
	s_mul_i32 s45, s30, 17
	s_add_i32 s46, s45, 17
	v_lshlrev_b64 v[40:41], 2, v[36:37]
	s_add_u32 s47, s20, 0x100000
	v_lshl_add_u64 v[42:43], s[4:5], 0, v[40:41]
	s_addc_u32 s48, s21, 0
	s_lshl_b64 s[40:41], s[38:39], 5
	s_lshl_b64 s[4:5], s[38:39], 12
	s_add_u32 s2, s2, s4
	v_or_b32_e32 v38, 0x80, v36
	v_lshlrev_b32_e32 v8, 2, v8
	s_addc_u32 s3, s3, s5
	v_ashrrev_i32_e32 v39, 31, v38
	v_lshl_add_u64 v[44:45], s[18:19], 0, v[40:41]
	v_lshl_add_u64 v[46:47], s[36:37], 0, v[10:11]
	v_xor_b32_e32 v103, 4, v8
	v_xor_b32_e32 v107, 8, v8
	v_xor_b32_e32 v113, 16, v8
	v_xor_b32_e32 v170, 32, v8
	v_xor_b32_e32 v171, 64, v8
	v_xor_b32_e32 v172, 0x80, v8
	v_lshl_add_u64 v[48:49], s[2:3], 0, v[40:41]
	v_lshl_add_u64 v[50:51], s[42:43], 0, v[10:11]
	global_load_dwordx4 v[182:185], v[42:43], off offset:16
	global_load_dwordx4 v[186:189], v[42:43], off
	global_load_dwordx4 v[194:197], v[44:45], off offset:16
	global_load_dwordx4 v[198:201], v[44:45], off
	global_load_dwordx4 v[202:205], v[42:43], off offset:528
	global_load_dwordx4 v[216:219], v[42:43], off offset:512
	global_load_dwordx4 v[220:223], v[44:45], off offset:528
	global_load_dwordx4 v[236:239], v[44:45], off offset:512
	s_mov_b32 s89, 1
	s_branch .LBB0_1690

; #define GAS __attribute__((address_space(1)))
; __device__ __forceinline__ const float* mod_ptr(const Frame& F, int l, int row) { return (const float*)(F.ws + WS_MOD) + ((size_t)l * 17 + row_b(row)) * 6144; }
; __device__ __forceinline__ void ph_ln2(Frame& F, int l, int ntok, bool last) {
;     ...
;     for (int row = gw; row < ntok; row += NGW) {
;         const Ln2Raw nxt = ln2_load(row + NGW < ntok ? row + NGW : row);
;         bf16_t* xr = (bf16_t*)(F.ws + WS_XR) + (size_t)row * DM;
;         const float* wg = (const float*)(F.ws + WS_WGT) + (size_t)row * 8;
;         const float* md = mod_ptr(F, l, row);
;         float ff[16];
; #pragma unroll
;         for (int e = 0; e < 16; ++e) ff[e] = 0.f;
;         { const unsigned a[4] = {cur.qs.x, cur.qs.y, cur.qs.z, cur.qs.w};
; #pragma unroll
;           for (int e = 0; e < 4; ++e) { const f32x2 lo = __builtin_amdgcn_cvt_pk_f32_fp8((int)a[e], false), hi = __builtin_amdgcn_cvt_pk_f32_fp8((int)a[e], true);
;               ff[4 * e] += pg8::Y2_INV * lo.x; ff[4 * e + 1] += pg8::Y2_INV * lo.y; ff[4 * e + 2] += pg8::Y2_INV * hi.x; ff[4 * e + 3] += pg8::Y2_INV * hi.y; } }
; #pragma unroll
;         for (int k = 0; k < 8; ++k) { const float wk = wg[k] * pg8::Y2_INV; const unsigned a[2] = {cur.q[k].x, cur.q[k].y};
; #pragma unroll
;             for (int h = 0; h < 2; ++h) {
;                 const f32x2 p0 = __builtin_amdgcn_cvt_scalef32_pk_f32_fp4(a[h], 1.0f, 0), p1 = __builtin_amdgcn_cvt_scalef32_pk_f32_fp4(a[h], 1.0f, 1), p2 = __builtin_amdgcn_cvt_scalef32_pk_f32_fp4(a[h], 1.0f, 2), p3 = __builtin_amdgcn_cvt_scalef32_pk_f32_fp4(a[h], 1.0f, 3);
;                 ff[8 * h] += wk * p0.x; ff[8 * h + 1] += wk * p0.y; ff[8 * h + 2] += wk * p1.x; ff[8 * h + 3] += wk * p1.y; ff[8 * h + 4] += wk * p2.x; ff[8 * h + 5] += wk * p2.y; ff[8 * h + 6] += wk * p3.x; ff[8 * h + 7] += wk * p3.y; } }
;     ...
;         for (int j = 0; j < 4; ++j) { const f32x4 g2 = *(const GAS f32x4*)(md + 5120 + LN2_COL(j));
.LBB0_1690:
	v_readlane_b32 s2, v255, 14
	s_mov_b32 s0, s38
	s_add_i32 s38, s38, s2
	s_cmp_ge_i32 s38, s80
	s_cselect_b64 s[42:43], -1, 0
	s_cmp_lt_i32 s38, s80
	v_readlane_b32 s3, v255, 15
	s_cselect_b32 s2, s38, s0
	s_ashr_i32 s3, s2, 31
	s_mul_i32 s4, s2, 0x1400
	s_mul_hi_i32 s5, s2, 0x1400
	s_add_u32 s4, s22, s4
	s_waitcnt vmcnt(0)
	v_mov_b64_e32 v[18:19], v[2:3]
	s_addc_u32 s5, s44, s5
	v_mov_b64_e32 v[16:17], v[0:1]
	v_lshl_add_u64 v[0:1], s[4:5], 0, v[34:35]
	v_mov_b64_e32 v[20:21], v[66:67]
	v_mov_b64_e32 v[22:23], v[64:65]
	v_mov_b64_e32 v[24:25], v[62:63]
	v_mov_b64_e32 v[26:27], v[60:61]
	v_mov_b64_e32 v[70:71], v[58:59]
	v_mov_b64_e32 v[28:29], v[56:57]
	v_mov_b64_e32 v[30:31], v[54:55]
	v_mov_b64_e32 v[68:69], v[52:53]
	global_load_dwordx2 v[52:53], v[0:1], off nt
	global_load_dwordx2 v[54:55], v[0:1], off offset:512 nt
	global_load_dwordx2 v[56:57], v[0:1], off offset:1024 nt
	global_load_dwordx2 v[58:59], v[0:1], off offset:1536 nt
	global_load_dwordx2 v[60:61], v[0:1], off offset:2048 nt
	global_load_dwordx2 v[62:63], v[0:1], off offset:2560 nt
	global_load_dwordx2 v[64:65], v[0:1], off offset:3072 nt
	global_load_dwordx2 v[66:67], v[0:1], off offset:3584 nt
	s_lshl_b64 s[2:3], s[2:3], 11
	v_lshl_add_u64 v[0:1], s[4:5], 0, v[32:33]
	s_movk_i32 s4, 0x1000
	v_add_co_u32_e32 v0, vcc, s4, v0
	s_add_u32 s4, s20, s40
	s_addc_u32 s5, s21, s41
	s_min_i32 s0, s0, 0x10000
	s_ashr_i32 s39, s0, 12
	s_ashr_i32 s49, s39, 31
	s_waitcnt lgkmcnt(0)
	v_lshl_add_u64 v[8:9], v[46:47], 0, s[2:3]
	s_add_u32 s2, s39, s45
	v_mov_b64_e32 v[74:75], v[6:7]
	s_addc_u32 s0, s49, 0
	v_mov_b64_e32 v[72:73], v[4:5]
	s_mulk_i32 s0, 0x6000
	s_mul_hi_u32 s3, s2, 0x6000
	v_addc_co_u32_e32 v1, vcc, 0, v1, vcc
	s_add_i32 s3, s3, s0
	v_cvt_pk_f32_fp8_e32 v[76:77], v72
	v_cvt_pk_f32_fp8_sdwa v[78:79], v72 src0_sel:WORD_1
	v_mov_b32_e32 v72, s4
	s_mov_b32 s0, 0x1a600000
	v_add_co_u32_e32 v98, vcc, s0, v72
	v_mov_b32_e32 v72, s5
	s_nop 0
	v_addc_co_u32_e32 v99, vcc, 0, v72, vcc
	global_load_dwordx4 v[4:7], v[0:1], off nt
	s_nop 0
	global_load_dwordx4 v[0:3], v[8:9], off nt
	s_nop 0
	global_load_dwordx4 v[8:11], v[8:9], off offset:256 nt
	v_cvt_pk_f32_fp8_e32 v[80:81], v73
	v_cvt_pk_f32_fp8_sdwa v[84:85], v73 src0_sel:WORD_1
	v_cvt_pk_f32_fp8_e32 v[88:89], v74
	v_cvt_pk_f32_fp8_sdwa v[92:93], v74 src0_sel:WORD_1
	v_cvt_pk_f32_fp8_e32 v[94:95], v75
	v_cvt_pk_f32_fp8_sdwa v[96:97], v75 src0_sel:WORD_1
	flat_load_dwordx4 v[72:75], v[98:99]
	s_mov_b32 s0, 0x3e000000
	v_cvt_scalef32_pk_f32_fp4 v[82:83], v68, 1.0
	v_pk_fma_f32 v[76:77], v[76:77], s[0:1], 0 op_sel_hi:[1,0,0]
	v_cvt_scalef32_pk_f32_fp4 v[86:87], v68, 1.0 op_sel:[1,0,0]
	v_cvt_scalef32_pk_f32_fp4 v[104:105], v68, 1.0 op_sel:[0,1,0]
	v_cvt_scalef32_pk_f32_fp4 v[108:109], v68, 1.0 op_sel:[1,1,0]
	v_cvt_scalef32_pk_f32_fp4 v[110:111], v69, 1.0
	v_cvt_scalef32_pk_f32_fp4 v[114:115], v69, 1.0 op_sel:[1,0,0]
	v_cvt_scalef32_pk_f32_fp4 v[116:117], v69, 1.0 op_sel:[0,1,0]
	v_cvt_scalef32_pk_f32_fp4 v[118:119], v69, 1.0 op_sel:[1,1,0]
	v_cvt_scalef32_pk_f32_fp4 v[68:69], v30, 1.0
	v_cvt_scalef32_pk_f32_fp4 v[90:91], v28, 1.0
	v_cvt_scalef32_pk_f32_fp4 v[130:131], v28, 1.0 op_sel:[1,0,0]
	v_cvt_scalef32_pk_f32_fp4 v[120:121], v30, 1.0 op_sel:[0,1,0]
	v_cvt_scalef32_pk_f32_fp4 v[132:133], v28, 1.0 op_sel:[0,1,0]
	v_cvt_scalef32_pk_f32_fp4 v[122:123], v30, 1.0 op_sel:[1,1,0]
	v_cvt_scalef32_pk_f32_fp4 v[124:125], v31, 1.0
	v_cvt_scalef32_pk_f32_fp4 v[134:135], v28, 1.0 op_sel:[1,1,0]
	v_cvt_scalef32_pk_f32_fp4 v[126:127], v31, 1.0 op_sel:[1,0,0]
	s_mulk_i32 s2, 0x6000
	v_cvt_scalef32_pk_f32_fp4 v[128:129], v31, 1.0 op_sel:[0,1,0]
	s_add_u32 s2, s47, s2
	s_addc_u32 s3, s48, s3
	s_add_u32 s36, s2, 0x5000
	s_addc_u32 s37, s3, 0
	s_cmp_eq_u32 s36, s89
	s_cbranch_scc1 .Lln2_g2_keep
	s_mov_b32 s89, s36
	v_lshl_add_u64 v[248:249], v[36:37], 2, s[36:37]
	v_lshl_add_u64 v[250:251], v[38:39], 2, s[36:37]
	global_load_dwordx4 v[206:209], v[248:249], off offset:16
	global_load_dwordx4 v[210:213], v[248:249], off
	global_load_dwordx4 v[240:243], v[250:251], off offset:16
	global_load_dwordx4 v[244:247], v[250:251], off
.Lln2_g2_keep:
	v_cvt_scalef32_pk_f32_fp4 v[162:163], v24, 1.0
	v_cvt_scalef32_pk_f32_fp4 v[154:155], v24, 1.0 op_sel:[1,0,0]
	v_cvt_scalef32_pk_f32_fp4 v[146:147], v24, 1.0 op_sel:[0,1,0]
	v_cvt_scalef32_pk_f32_fp4 v[138:139], v24, 1.0 op_sel:[1,1,0]
	v_cvt_scalef32_pk_f32_fp4 v[158:159], v26, 1.0
	v_cvt_scalef32_pk_f32_fp4 v[150:151], v26, 1.0 op_sel:[1,0,0]
	v_cvt_scalef32_pk_f32_fp4 v[142:143], v26, 1.0 op_sel:[0,1,0]
	v_cvt_scalef32_pk_f32_fp4 v[166:167], v22, 1.0
	v_cvt_scalef32_pk_f32_fp4 v[160:161], v22, 1.0 op_sel:[1,0,0]
	v_cvt_scalef32_pk_f32_fp4 v[152:153], v22, 1.0 op_sel:[0,1,0]
	v_cvt_scalef32_pk_f32_fp4 v[144:145], v22, 1.0 op_sel:[1,1,0]
	v_cvt_scalef32_pk_f32_fp4 v[136:137], v23, 1.0
	v_cvt_scalef32_pk_f32_fp4 v[168:169], v20, 1.0
	v_cvt_scalef32_pk_f32_fp4 v[164:165], v20, 1.0 op_sel:[1,0,0]
	v_cvt_scalef32_pk_f32_fp4 v[156:157], v20, 1.0 op_sel:[0,1,0]
	v_cvt_scalef32_pk_f32_fp4 v[148:149], v20, 1.0 op_sel:[1,1,0]
	v_cvt_scalef32_pk_f32_fp4 v[140:141], v21, 1.0
	v_lshl_add_u64 v[178:179], v[38:39], 2, s[36:37]
	v_readlane_b32 s4, v255, 32
	v_readlane_b32 s5, v255, 33
	s_andn2_b64 vcc, exec, s[4:5]
	s_waitcnt vmcnt(0) lgkmcnt(0)
; #define GAS __attribute__((address_space(1)))
; __device__ __forceinline__ void unpack8(const u32x4 q, float* o) { o[0] = bflo(q.x); o[1] = bfhi(q.x); o[2] = bflo(q.y); o[3] = bfhi(q.y); o[4] = bflo(q.z); o[5] = bfhi(q.z); o[6] = bflo(q.w); o[7] = bfhi(q.w); }
; __device__ __forceinline__ void ph_ln2(Frame& F, int l, int ntok, bool last) {
;     ...
;         { const unsigned a[4] = {cur.qs.x, cur.qs.y, cur.qs.z, cur.qs.w};
; #pragma unroll
;           for (int e = 0; e < 4; ++e) { const f32x2 lo = __builtin_amdgcn_cvt_pk_f32_fp8((int)a[e], false), hi = __builtin_amdgcn_cvt_pk_f32_fp8((int)a[e], true);
;               ff[4 * e] += pg8::Y2_INV * lo.x; ff[4 * e + 1] += pg8::Y2_INV * lo.y; ff[4 * e + 2] += pg8::Y2_INV * hi.x; ff[4 * e + 3] += pg8::Y2_INV * hi.y; } }
; #pragma unroll
;         for (int k = 0; k < 8; ++k) { const float wk = wg[k] * pg8::Y2_INV; const unsigned a[2] = {cur.q[k].x, cur.q[k].y};
; #pragma unroll
;             for (int h = 0; h < 2; ++h) {
;                 const f32x2 p0 = __builtin_amdgcn_cvt_scalef32_pk_f32_fp4(a[h], 1.0f, 0), p1 = __builtin_amdgcn_cvt_scalef32_pk_f32_fp4(a[h], 1.0f, 1), p2 = __builtin_amdgcn_cvt_scalef32_pk_f32_fp4(a[h], 1.0f, 2), p3 = __builtin_amdgcn_cvt_scalef32_pk_f32_fp4(a[h], 1.0f, 3);
;                 ff[8 * h] += wk * p0.x; ff[8 * h + 1] += wk * p0.y; ff[8 * h + 2] += wk * p1.x; ff[8 * h + 3] += wk * p1.y; ff[8 * h + 4] += wk * p2.x; ff[8 * h + 5] += wk * p2.y; ff[8 * h + 6] += wk * p3.x; ff[8 * h + 7] += wk * p3.y; } }
;         float v[16], xo[16]; float s = 0.f;
;         unpack8(cur.xa, xo); unpack8(cur.xb, xo + 8);
; #pragma unroll
;         for (int j = 0; j < 4; ++j) { const f32x4 g2 = *(const GAS f32x4*)(md + 5120 + LN2_COL(j));
; #pragma unroll
;             for (int e = 0; e < 4; ++e) { v[4 * j + e] = xo[4 * j + e] * DN_ALPHA + g2[e] * ff[4 * j + e]; s += v[4 * j + e]; } }
	v_mul_f32_e32 v100, 0x3e000000, v72
	v_mul_f32_e32 v102, 0x3e000000, v73
	v_pk_fma_f32 v[76:77], v[100:101], v[82:83], v[76:77] op_sel_hi:[0,1,1]
	v_mul_f32_e32 v74, 0x3e000000, v74
	v_pk_fma_f32 v[68:69], v[102:103], v[68:69], v[76:77] op_sel_hi:[0,1,1]
	v_pk_fma_f32 v[90:91], v[74:75], v[90:91], v[68:69] op_sel_hi:[0,1,1]
	v_pk_fma_f32 v[68:69], v[78:79], s[0:1], 0 op_sel_hi:[1,0,0]
	v_cvt_scalef32_pk_f32_fp4 v[72:73], v30, 1.0 op_sel:[1,0,0]
	v_pk_fma_f32 v[68:69], v[100:101], v[86:87], v[68:69] op_sel_hi:[0,1,1]
	v_pk_fma_f32 v[68:69], v[102:103], v[72:73], v[68:69] op_sel_hi:[0,1,1]
	v_pk_fma_f32 v[86:87], v[74:75], v[130:131], v[68:69] op_sel_hi:[0,1,1]
	v_pk_fma_f32 v[68:69], v[80:81], s[0:1], 0 op_sel_hi:[1,0,0]
	v_pk_fma_f32 v[76:77], v[88:89], s[0:1], 0 op_sel_hi:[1,0,0]
	v_pk_fma_f32 v[68:69], v[100:101], v[104:105], v[68:69] op_sel_hi:[0,1,1]
	v_pk_fma_f32 v[68:69], v[102:103], v[120:121], v[68:69] op_sel_hi:[0,1,1]
	v_pk_fma_f32 v[82:83], v[74:75], v[132:133], v[68:69] op_sel_hi:[0,1,1]
	v_pk_fma_f32 v[68:69], v[84:85], s[0:1], 0 op_sel_hi:[1,0,0]
	v_pk_fma_f32 v[76:77], v[100:101], v[110:111], v[76:77] op_sel_hi:[0,1,1]
	v_pk_fma_f32 v[68:69], v[100:101], v[108:109], v[68:69] op_sel_hi:[0,1,1]
	v_pk_fma_f32 v[68:69], v[102:103], v[122:123], v[68:69] op_sel_hi:[0,1,1]
	v_pk_fma_f32 v[80:81], v[74:75], v[134:135], v[68:69] op_sel_hi:[0,1,1]
	v_cvt_scalef32_pk_f32_fp4 v[68:69], v29, 1.0
	v_pk_fma_f32 v[76:77], v[102:103], v[124:125], v[76:77] op_sel_hi:[0,1,1]
	v_pk_fma_f32 v[76:77], v[74:75], v[68:69], v[76:77] op_sel_hi:[0,1,1]
	v_pk_fma_f32 v[68:69], v[92:93], s[0:1], 0 op_sel_hi:[1,0,0]
	v_cvt_scalef32_pk_f32_fp4 v[72:73], v29, 1.0 op_sel:[1,0,0]
	v_pk_fma_f32 v[68:69], v[100:101], v[114:115], v[68:69] op_sel_hi:[0,1,1]
	v_pk_fma_f32 v[68:69], v[102:103], v[126:127], v[68:69] op_sel_hi:[0,1,1]
	v_pk_fma_f32 v[72:73], v[74:75], v[72:73], v[68:69] op_sel_hi:[0,1,1]
	v_pk_fma_f32 v[68:69], v[94:95], s[0:1], 0 op_sel_hi:[1,0,0]
	v_cvt_scalef32_pk_f32_fp4 v[78:79], v29, 1.0 op_sel:[0,1,0]
	v_pk_fma_f32 v[68:69], v[100:101], v[116:117], v[68:69] op_sel_hi:[0,1,1]
	flat_load_dwordx4 v[114:117], v[98:99] offset:16
	v_pk_fma_f32 v[68:69], v[102:103], v[128:129], v[68:69] op_sel_hi:[0,1,1]
	v_pk_fma_f32 v[68:69], v[74:75], v[78:79], v[68:69] op_sel_hi:[0,1,1]
	v_pk_fma_f32 v[78:79], v[96:97], s[0:1], 0 op_sel_hi:[1,0,0]
	v_cvt_scalef32_pk_f32_fp4 v[30:31], v31, 1.0 op_sel:[1,1,0]
	v_pk_fma_f32 v[78:79], v[100:101], v[118:119], v[78:79] op_sel_hi:[0,1,1]
	v_pk_fma_f32 v[30:31], v[102:103], v[30:31], v[78:79] op_sel_hi:[0,1,1]
	v_cvt_scalef32_pk_f32_fp4 v[130:131], v25, 1.0
	v_cvt_scalef32_pk_f32_fp4 v[122:123], v25, 1.0 op_sel:[1,0,0]
	v_cvt_scalef32_pk_f32_fp4 v[104:105], v25, 1.0 op_sel:[1,1,0]
	v_cvt_scalef32_pk_f32_fp4 v[134:135], v26, 1.0 op_sel:[1,1,0]
	v_cvt_scalef32_pk_f32_fp4 v[126:127], v27, 1.0
	v_cvt_scalef32_pk_f32_fp4 v[118:119], v27, 1.0 op_sel:[1,0,0]
	v_cvt_scalef32_pk_f32_fp4 v[108:109], v27, 1.0 op_sel:[0,1,0]
	v_cvt_scalef32_pk_f32_fp4 v[100:101], v27, 1.0 op_sel:[1,1,0]
	v_cvt_scalef32_pk_f32_fp4 v[128:129], v23, 1.0 op_sel:[1,0,0]
	v_cvt_scalef32_pk_f32_fp4 v[120:121], v23, 1.0 op_sel:[0,1,0]
	v_cvt_scalef32_pk_f32_fp4 v[110:111], v23, 1.0 op_sel:[1,1,0]
	v_cvt_scalef32_pk_f32_fp4 v[132:133], v21, 1.0 op_sel:[1,0,0]
	v_cvt_scalef32_pk_f32_fp4 v[124:125], v21, 1.0 op_sel:[0,1,0]
	v_cvt_scalef32_pk_f32_fp4 v[28:29], v29, 1.0 op_sel:[1,1,0]
	v_pk_fma_f32 v[28:29], v[74:75], v[28:29], v[30:31] op_sel_hi:[0,1,1]
	v_mul_f32_e32 v30, 0x3e000000, v75
	v_cvt_scalef32_pk_f32_fp4 v[96:97], v70, 1.0
	v_pk_fma_f32 v[90:91], v[30:31], v[96:97], v[90:91] op_sel_hi:[0,1,1]
	v_lshlrev_b32_e32 v96, 16, v16
	v_and_b32_e32 v97, 0xffff0000, v16
	s_mov_b32 s0, 0x3fd744fd
	v_cvt_scalef32_pk_f32_fp4 v[94:95], v70, 1.0 op_sel:[1,0,0]
	v_cvt_scalef32_pk_f32_fp4 v[92:93], v70, 1.0 op_sel:[0,1,0]
	v_cvt_scalef32_pk_f32_fp4 v[88:89], v70, 1.0 op_sel:[1,1,0]
	v_cvt_scalef32_pk_f32_fp4 v[84:85], v71, 1.0
	v_cvt_scalef32_pk_f32_fp4 v[78:79], v71, 1.0 op_sel:[1,0,0]
	v_cvt_scalef32_pk_f32_fp4 v[74:75], v71, 1.0 op_sel:[0,1,0]
	v_cvt_scalef32_pk_f32_fp4 v[70:71], v71, 1.0 op_sel:[1,1,0]
	s_waitcnt vmcnt(0) lgkmcnt(0)
	v_mul_f32_e32 v98, 0x3e000000, v114
	v_mul_f32_e32 v102, 0x3e000000, v115
	v_cvt_scalef32_pk_f32_fp4 v[114:115], v25, 1.0 op_sel:[0,1,0]
	v_lshl_add_u64 v[24:25], v[36:37], 2, s[36:37]
	v_mul_f32_e32 v106, 0x3e000000, v116
	v_mul_f32_e32 v112, 0x3e000000, v117
	v_cvt_scalef32_pk_f32_fp4 v[116:117], v21, 1.0 op_sel:[1,1,0]
	v_mov_b32_e32 v20, v206
	v_mov_b32_e32 v21, v207
	v_mov_b32_e32 v22, v208
	v_mov_b32_e32 v23, v209
	s_nop 0
	v_mov_b32_e32 v24, v210
	v_mov_b32_e32 v25, v211
	v_mov_b32_e32 v26, v212
	v_mov_b32_e32 v27, v213
	s_nop 0
	v_mov_b32_e32 v174, v240
	v_mov_b32_e32 v175, v241
	v_mov_b32_e32 v176, v242
	v_mov_b32_e32 v177, v243
	s_nop 0
	v_mov_b32_e32 v178, v244
	v_mov_b32_e32 v179, v245
	v_mov_b32_e32 v180, v246
	v_mov_b32_e32 v181, v247
	v_pk_fma_f32 v[90:91], v[98:99], v[158:159], v[90:91] op_sel_hi:[0,1,1]
	v_pk_fma_f32 v[90:91], v[102:103], v[162:163], v[90:91] op_sel_hi:[0,1,1]
	v_pk_fma_f32 v[90:91], v[106:107], v[166:167], v[90:91] op_sel_hi:[0,1,1]
	v_pk_fma_f32 v[90:91], v[112:113], v[168:169], v[90:91] op_sel_hi:[0,1,1]
	s_waitcnt vmcnt(2)
; #define GAS __attribute__((address_space(1)))
; __device__ __forceinline__ void unpack8(const u32x4 q, float* o) { o[0] = bflo(q.x); o[1] = bfhi(q.x); o[2] = bflo(q.y); o[3] = bfhi(q.y); o[4] = bflo(q.z); o[5] = bfhi(q.z); o[6] = bflo(q.w); o[7] = bfhi(q.w); }
; __device__ __forceinline__ void ph_ln2(Frame& F, int l, int ntok, bool last) {
;     ...
;         for (int k = 0; k < 8; ++k) { const float wk = wg[k] * pg8::Y2_INV; const unsigned a[2] = {cur.q[k].x, cur.q[k].y};
; #pragma unroll
;             for (int h = 0; h < 2; ++h) {
;                 const f32x2 p0 = __builtin_amdgcn_cvt_scalef32_pk_f32_fp4(a[h], 1.0f, 0), p1 = __builtin_amdgcn_cvt_scalef32_pk_f32_fp4(a[h], 1.0f, 1), p2 = __builtin_amdgcn_cvt_scalef32_pk_f32_fp4(a[h], 1.0f, 2), p3 = __builtin_amdgcn_cvt_scalef32_pk_f32_fp4(a[h], 1.0f, 3);
;                 ff[8 * h] += wk * p0.x; ff[8 * h + 1] += wk * p0.y; ff[8 * h + 2] += wk * p1.x; ff[8 * h + 3] += wk * p1.y; ff[8 * h + 4] += wk * p2.x; ff[8 * h + 5] += wk * p2.y; ff[8 * h + 6] += wk * p3.x; ff[8 * h + 7] += wk * p3.y; } }
;         float v[16], xo[16]; float s = 0.f;
;         unpack8(cur.xa, xo); unpack8(cur.xb, xo + 8);
; #pragma unroll
;         for (int j = 0; j < 4; ++j) { const f32x4 g2 = *(const GAS f32x4*)(md + 5120 + LN2_COL(j));
; #pragma unroll
;             for (int e = 0; e < 4; ++e) { v[4 * j + e] = xo[4 * j + e] * DN_ALPHA + g2[e] * ff[4 * j + e]; s += v[4 * j + e]; } }
;         const float mean = wave_sum(s, F.lane) * (1.f / DM); float s2 = 0.f;
; #pragma unroll
;         for (int e = 0; e < 16; ++e) { v[e] -= mean; s2 += v[e] * v[e]; }
;         const float rstd = 1.f / sqrtf(wave_sum(s2, F.lane) * (1.f / DM) + LN_EPS);
	v_pk_mul_f32 v[24:25], v[90:91], v[24:25]
	s_nop 0
	v_pk_fma_f32 v[24:25], v[96:97], s[0:1], v[24:25] op_sel_hi:[1,0,1]
	s_nop 0
	v_add_f32_e32 v16, 0, v24
	v_add_f32_e32 v31, v25, v16
	v_pk_fma_f32 v[86:87], v[30:31], v[94:95], v[86:87] op_sel_hi:[0,1,1]
	v_pk_fma_f32 v[86:87], v[98:99], v[150:151], v[86:87] op_sel_hi:[0,1,1]
	v_pk_fma_f32 v[86:87], v[102:103], v[154:155], v[86:87] op_sel_hi:[0,1,1]
	v_pk_fma_f32 v[86:87], v[106:107], v[160:161], v[86:87] op_sel_hi:[0,1,1]
	v_pk_fma_f32 v[86:87], v[112:113], v[164:165], v[86:87] op_sel_hi:[0,1,1]
	v_lshlrev_b32_e32 v16, 16, v17
	v_and_b32_e32 v17, 0xffff0000, v17
	v_pk_mul_f32 v[26:27], v[86:87], v[26:27]
	s_nop 0
	v_pk_fma_f32 v[16:17], v[16:17], s[0:1], v[26:27] op_sel_hi:[1,0,1]
	s_nop 0
	v_add_f32_e32 v26, v16, v31
	v_add_f32_e32 v31, v17, v26
	v_pk_fma_f32 v[26:27], v[30:31], v[92:93], v[82:83] op_sel_hi:[0,1,1]
	v_pk_fma_f32 v[26:27], v[98:99], v[142:143], v[26:27] op_sel_hi:[0,1,1]
	v_pk_fma_f32 v[26:27], v[102:103], v[146:147], v[26:27] op_sel_hi:[0,1,1]
	v_pk_fma_f32 v[26:27], v[106:107], v[152:153], v[26:27] op_sel_hi:[0,1,1]
	v_pk_fma_f32 v[26:27], v[112:113], v[156:157], v[26:27] op_sel_hi:[0,1,1]
	v_lshlrev_b32_e32 v82, 16, v18
	v_and_b32_e32 v83, 0xffff0000, v18
	v_pk_mul_f32 v[20:21], v[26:27], v[20:21]
	s_nop 0
	v_pk_fma_f32 v[20:21], v[82:83], s[0:1], v[20:21] op_sel_hi:[1,0,1]
	s_nop 0
	v_add_f32_e32 v18, v20, v31
	v_add_f32_e32 v31, v21, v18
	v_pk_fma_f32 v[26:27], v[30:31], v[88:89], v[80:81] op_sel_hi:[0,1,1]
	v_pk_fma_f32 v[26:27], v[98:99], v[134:135], v[26:27] op_sel_hi:[0,1,1]
	v_pk_fma_f32 v[26:27], v[102:103], v[138:139], v[26:27] op_sel_hi:[0,1,1]
	v_pk_fma_f32 v[26:27], v[106:107], v[144:145], v[26:27] op_sel_hi:[0,1,1]
	v_pk_fma_f32 v[26:27], v[112:113], v[148:149], v[26:27] op_sel_hi:[0,1,1]
	v_lshlrev_b32_e32 v18, 16, v19
	v_and_b32_e32 v19, 0xffff0000, v19
	v_pk_mul_f32 v[22:23], v[26:27], v[22:23]
	v_lshlrev_b32_e32 v26, 16, v12
	v_pk_fma_f32 v[18:19], v[18:19], s[0:1], v[22:23] op_sel_hi:[1,0,1]
	v_and_b32_e32 v27, 0xffff0000, v12
	v_add_f32_e32 v22, v18, v31
	v_add_f32_e32 v31, v19, v22
	v_pk_fma_f32 v[22:23], v[30:31], v[84:85], v[76:77] op_sel_hi:[0,1,1]
	v_pk_fma_f32 v[22:23], v[98:99], v[126:127], v[22:23] op_sel_hi:[0,1,1]
	v_pk_fma_f32 v[22:23], v[102:103], v[130:131], v[22:23] op_sel_hi:[0,1,1]
	v_pk_fma_f32 v[22:23], v[106:107], v[136:137], v[22:23] op_sel_hi:[0,1,1]
	v_pk_fma_f32 v[22:23], v[112:113], v[140:141], v[22:23] op_sel_hi:[0,1,1]
	s_waitcnt vmcnt(0)
	v_pk_mul_f32 v[22:23], v[22:23], v[178:179]
	s_nop 0
	v_pk_fma_f32 v[22:23], v[26:27], s[0:1], v[22:23] op_sel_hi:[1,0,1]
	s_nop 0
	v_add_f32_e32 v12, v22, v31
	v_add_f32_e32 v31, v23, v12
	v_pk_fma_f32 v[26:27], v[30:31], v[78:79], v[72:73] op_sel_hi:[0,1,1]
	v_pk_fma_f32 v[26:27], v[98:99], v[118:119], v[26:27] op_sel_hi:[0,1,1]
	v_pk_fma_f32 v[26:27], v[102:103], v[122:123], v[26:27] op_sel_hi:[0,1,1]
	v_pk_fma_f32 v[26:27], v[106:107], v[128:129], v[26:27] op_sel_hi:[0,1,1]
	v_pk_fma_f32 v[26:27], v[112:113], v[132:133], v[26:27] op_sel_hi:[0,1,1]
	v_lshlrev_b32_e32 v12, 16, v13
	v_and_b32_e32 v13, 0xffff0000, v13
	v_pk_mul_f32 v[26:27], v[26:27], v[180:181]
	s_nop 0
	v_pk_fma_f32 v[72:73], v[12:13], s[0:1], v[26:27] op_sel_hi:[1,0,1]
	v_lshlrev_b32_e32 v26, 16, v14
	v_add_f32_e32 v12, v72, v31
	v_add_f32_e32 v31, v73, v12
	v_pk_fma_f32 v[12:13], v[30:31], v[74:75], v[68:69] op_sel_hi:[0,1,1]
	v_pk_fma_f32 v[12:13], v[98:99], v[108:109], v[12:13] op_sel_hi:[0,1,1]
	v_pk_fma_f32 v[12:13], v[102:103], v[114:115], v[12:13] op_sel_hi:[0,1,1]
	v_pk_fma_f32 v[12:13], v[106:107], v[120:121], v[12:13] op_sel_hi:[0,1,1]
	v_pk_fma_f32 v[12:13], v[112:113], v[124:125], v[12:13] op_sel_hi:[0,1,1]
	v_and_b32_e32 v27, 0xffff0000, v14
	v_pk_mul_f32 v[12:13], v[12:13], v[174:175]
	v_lshlrev_b32_e32 v14, 16, v15
	v_pk_fma_f32 v[68:69], v[26:27], s[0:1], v[12:13] op_sel_hi:[1,0,1]
	v_and_b32_e32 v15, 0xffff0000, v15
	v_add_f32_e32 v12, v68, v31
	v_add_f32_e32 v26, v69, v12
	v_pk_fma_f32 v[12:13], v[30:31], v[70:71], v[28:29] op_sel_hi:[0,1,1]
	v_pk_fma_f32 v[12:13], v[98:99], v[100:101], v[12:13] op_sel_hi:[0,1,1]
	v_pk_fma_f32 v[12:13], v[102:103], v[104:105], v[12:13] op_sel_hi:[0,1,1]
	v_pk_fma_f32 v[12:13], v[106:107], v[110:111], v[12:13] op_sel_hi:[0,1,1]
	v_pk_fma_f32 v[12:13], v[112:113], v[116:117], v[12:13] op_sel_hi:[0,1,1]
	v_pk_mul_f32 v[12:13], v[12:13], v[176:177]
	s_nop 0
	v_pk_fma_f32 v[30:31], v[14:15], s[0:1], v[12:13] op_sel_hi:[1,0,1]
	s_nop 0
	v_add_f32_e32 v12, v30, v26
	v_add_f32_e32 v12, v31, v12
	ds_bpermute_b32 v13, v103, v12
	s_waitcnt lgkmcnt(0)
	v_add_f32_e32 v12, v12, v13
	ds_bpermute_b32 v13, v107, v12
	s_waitcnt lgkmcnt(0)
	v_add_f32_e32 v12, v12, v13
	ds_bpermute_b32 v13, v113, v12
	s_waitcnt lgkmcnt(0)
	v_add_f32_e32 v12, v12, v13
	ds_bpermute_b32 v13, v170, v12
	s_waitcnt lgkmcnt(0)
	v_add_f32_e32 v12, v12, v13
	ds_bpermute_b32 v13, v171, v12
	s_waitcnt lgkmcnt(0)
	v_add_f32_e32 v12, v12, v13
	ds_bpermute_b32 v13, v172, v12
	s_waitcnt lgkmcnt(0)
	v_add_f32_e32 v12, v12, v13
	v_mul_f32_e32 v70, 0x3a800000, v12
	v_pk_add_f32 v[12:13], v[24:25], v[70:71] op_sel_hi:[1,0] neg_lo:[0,1] neg_hi:[0,1]
	v_pk_add_f32 v[14:15], v[16:17], v[70:71] op_sel_hi:[1,0] neg_lo:[0,1] neg_hi:[0,1]
	v_pk_mul_f32 v[74:75], v[12:13], v[12:13]
	v_pk_mul_f32 v[16:17], v[14:15], v[14:15]
	v_add_f32_e32 v74, v74, v75
	v_pk_add_f32 v[24:25], v[20:21], v[70:71] op_sel_hi:[1,0] neg_lo:[0,1] neg_hi:[0,1]
	v_add_f32_e32 v16, v16, v74
	v_pk_mul_f32 v[76:77], v[24:25], v[24:25]
	v_add_f32_e32 v16, v17, v16
	v_pk_add_f32 v[26:27], v[18:19], v[70:71] op_sel_hi:[1,0] neg_lo:[0,1] neg_hi:[0,1]
	v_add_f32_e32 v16, v76, v16
	v_pk_mul_f32 v[18:19], v[26:27], v[26:27]
	v_add_f32_e32 v16, v77, v16
	v_pk_add_f32 v[20:21], v[22:23], v[70:71] op_sel_hi:[1,0] neg_lo:[0,1] neg_hi:[0,1]
	v_add_f32_e32 v16, v18, v16
	v_pk_mul_f32 v[78:79], v[20:21], v[20:21]
	v_add_f32_e32 v16, v19, v16
	v_pk_add_f32 v[22:23], v[72:73], v[70:71] op_sel_hi:[1,0] neg_lo:[0,1] neg_hi:[0,1]
	v_add_f32_e32 v16, v78, v16
	v_pk_mul_f32 v[72:73], v[22:23], v[22:23]
	v_add_f32_e32 v16, v79, v16
	v_pk_add_f32 v[28:29], v[68:69], v[70:71] op_sel_hi:[1,0] neg_lo:[0,1] neg_hi:[0,1]
	v_add_f32_e32 v16, v72, v16
	v_pk_mul_f32 v[68:69], v[28:29], v[28:29]
	v_add_f32_e32 v16, v73, v16
	v_pk_add_f32 v[30:31], v[30:31], v[70:71] op_sel_hi:[1,0] neg_lo:[0,1] neg_hi:[0,1]
	v_add_f32_e32 v16, v68, v16
	v_pk_mul_f32 v[70:71], v[30:31], v[30:31]
	v_add_f32_e32 v16, v69, v16
	v_add_f32_e32 v16, v70, v16
	v_add_f32_e32 v16, v71, v16
	ds_bpermute_b32 v17, v103, v16
	s_waitcnt lgkmcnt(0)
	v_add_f32_e32 v16, v16, v17
	ds_bpermute_b32 v17, v107, v16
	s_waitcnt lgkmcnt(0)
	v_add_f32_e32 v16, v16, v17
	ds_bpermute_b32 v17, v113, v16
	s_waitcnt lgkmcnt(0)
	v_add_f32_e32 v16, v16, v17
	ds_bpermute_b32 v17, v170, v16
	s_waitcnt lgkmcnt(0)
	v_add_f32_e32 v16, v16, v17
	ds_bpermute_b32 v17, v171, v16
	s_waitcnt lgkmcnt(0)
	v_add_f32_e32 v16, v16, v17
	ds_bpermute_b32 v17, v172, v16
	s_cbranch_vccnz .LBB0_1692
; __device__ __forceinline__ const float* mod_ptr(const Frame& F, int l, int row) { return (const float*)(F.ws + WS_MOD) + ((size_t)l * 17 + row_b(row)) * 6144; }
; __device__ __forceinline__ void ph_ln2(Frame& F, int l, int ntok, bool last) {
;     ...
;         const float* mdn = last ? md : mod_ptr(F, l + 1, row);
	s_add_u32 s0, s39, s46
	s_addc_u32 s2, s49, 0
	s_mulk_i32 s2, 0x6000
	s_mul_hi_u32 s3, s0, 0x6000
	s_add_i32 s3, s3, s2
	s_mulk_i32 s0, 0x6000
	s_add_u32 s2, s47, s0
	s_addc_u32 s3, s48, s3
